# v37 + MLA first-half step: exp2/fp8-pack block moved behind the third QK MFMA in place of the 20 wait-state nops (not interleaved between the chained MFMAs)
# baseline (speedup 1.0000x reference)
.LBB0_570:
	s_waitcnt lgkmcnt(4)
	v_mfma_scale_f32_32x32x64_f8f6f4 v[80:95], v[80:87], v[120:127], 0, v205, v205 op_sel_hi:[0,0,0]
	s_mov_b64 s[4:5], exec
	s_cmp_ge_u32 s18, s20
	s_waitcnt lgkmcnt(2)
	v_mfma_scale_f32_32x32x64_f8f6f4 v[80:95], v[104:111], v[128:135], v[80:95], v205, v205 op_sel_hi:[0,0,0]
	s_waitcnt lgkmcnt(0)
	v_mfma_scale_f32_32x32x64_f8f6f4 v[80:95], v[96:103], v[136:143], v[80:95], v205, v205 op_sel_hi:[0,0,0]
	v_exp_f32_e32 v224, v178
	v_exp_f32_e32 v225, v179
	v_exp_f32_e32 v226, v176
	v_exp_f32_e32 v227, v177
	v_exp_f32_e32 v228, v162
	v_exp_f32_e32 v229, v163
	v_exp_f32_e32 v230, v160
	v_exp_f32_e32 v231, v161
	v_exp_f32_e32 v232, v158
	v_exp_f32_e32 v233, v159
	v_exp_f32_e32 v234, v156
	v_exp_f32_e32 v235, v157
	v_exp_f32_e32 v236, v154
	v_exp_f32_e32 v237, v155
	v_exp_f32_e32 v238, v152
	v_exp_f32_e32 v239, v153
	v_mov_b32_e32 v144, 0
	v_mov_b32_e32 v145, 0
	v_mov_b32_e32 v146, 0
	v_mov_b32_e32 v147, 0
	v_cvt_pk_fp8_f32 v144, v224, v225
	v_cvt_pk_fp8_f32 v145, v228, v229
	v_cvt_pk_fp8_f32 v146, v232, v233
	v_cvt_pk_fp8_f32 v147, v236, v237
	v_cvt_pk_fp8_f32 v144, v226, v227 op_sel:[0,0,1]
	v_cvt_pk_fp8_f32 v145, v230, v231 op_sel:[0,0,1]
	v_cvt_pk_fp8_f32 v146, v234, v235 op_sel:[0,0,1]
	v_cvt_pk_fp8_f32 v147, v238, v239 op_sel:[0,0,1]
	v_max_f32_e32 v96, v81, v81
	v_max_f32_e32 v97, v80, v80
	v_max_f32_e32 v96, v97, v96
	v_max3_f32 v96, v96, v82, v83
	v_max3_f32 v96, v96, v84, v85
	v_max3_f32 v96, v96, v86, v87
	v_max3_f32 v96, v96, v88, v89
	v_max3_f32 v96, v96, v90, v91
	v_max3_f32 v96, v96, v92, v93
	v_max3_f32 v96, v96, v94, v95
	v_mov_b32_e32 v97, v96
	s_nop 1
	v_permlane32_swap_b32_e32 v96, v97
	v_max_f32_e32 v97, v97, v97
	v_max_f32_e32 v96, v96, v96
	v_max_f32_e32 v96, v96, v97
	v_fma_f32 v97, v96, s40, -v192
	v_cmp_ge_f32_e32 vcc, s70, v97
	s_cbranch_scc1 .LBB0_577
	s_xor_b32 s25, s23, 1
	s_lshl_b32 s18, s25, 15
	s_add_i32 s26, s18, 0
	v_add3_u32 v97, s26, v212, v190
	s_waitcnt vmcnt(1)
	ds_write_b128 v97, v[168:171]
	s_and_saveexec_b64 s[18:19], s[0:1]
	v_add3_u32 v97, s26, v215, v188
	ds_write_b128 v97, v[164:167]
	s_or_b64 exec, exec, s[18:19]
	v_lshl_add_u32 v97, s25, 14, v207
	s_cmp_ge_u32 s78, s74
	s_waitcnt vmcnt(0)
	ds_write_b128 v97, v[172:175]
	s_cbranch_scc1 .LBB0_577
	s_cmp_lt_u32 s78, s77
	s_cselect_b32 s18, 0, s77
	s_cselect_b32 s19, s76, s75
	s_lshl_b32 s18, s18, 6
	s_sub_i32 s25, s19, s18
	s_add_i32 s25, s25, s22
	v_add_u32_e32 v97, s25, v210
	v_mad_i64_i32 v[98:99], s[18:19], v97, s64, v[194:195]
	global_load_dwordx4 v[168:171], v[98:99], off
	s_and_saveexec_b64 s[18:19], s[0:1]
	s_cbranch_execz .LBB0_576
	v_add_u32_e32 v97, s25, v213
	v_mad_i64_i32 v[98:99], s[26:27], v97, s64, v[196:197]
	global_load_dwordx4 v[164:167], v[98:99], off

.LBB0_1880:
	s_waitcnt lgkmcnt(4)
	v_mfma_scale_f32_32x32x64_f8f6f4 v[80:95], v[80:87], v[120:127], 0, v207, v207 op_sel_hi:[0,0,0]
	s_xor_b32 s22, s24, 1
	s_lshl_b32 s18, s22, 15
	s_add_i32 s23, s18, 0
	s_mov_b64 s[20:21], exec
	s_waitcnt lgkmcnt(2)
	v_mfma_scale_f32_32x32x64_f8f6f4 v[80:95], v[104:111], v[128:135], v[80:95], v207, v207 op_sel_hi:[0,0,0]
	s_waitcnt lgkmcnt(0)
	v_mfma_scale_f32_32x32x64_f8f6f4 v[80:95], v[96:103], v[136:143], v[80:95], v207, v207 op_sel_hi:[0,0,0]
	v_exp_f32_e32 v224, v178
	v_exp_f32_e32 v225, v179
	v_exp_f32_e32 v226, v176
	v_exp_f32_e32 v227, v177
	v_exp_f32_e32 v228, v162
	v_exp_f32_e32 v229, v163
	v_exp_f32_e32 v230, v160
	v_exp_f32_e32 v231, v161
	v_exp_f32_e32 v232, v158
	v_exp_f32_e32 v233, v159
	v_exp_f32_e32 v234, v156
	v_exp_f32_e32 v235, v157
	v_exp_f32_e32 v236, v154
	v_exp_f32_e32 v237, v155
	v_exp_f32_e32 v238, v152
	v_exp_f32_e32 v239, v153
	v_mov_b32_e32 v144, 0
	v_mov_b32_e32 v145, 0
	v_mov_b32_e32 v146, 0
	v_mov_b32_e32 v147, 0
	v_cvt_pk_fp8_f32 v144, v224, v225
	v_cvt_pk_fp8_f32 v145, v228, v229
	v_cvt_pk_fp8_f32 v146, v232, v233
	v_cvt_pk_fp8_f32 v147, v236, v237
	v_cvt_pk_fp8_f32 v144, v226, v227 op_sel:[0,0,1]
	v_cvt_pk_fp8_f32 v145, v230, v231 op_sel:[0,0,1]
	v_cvt_pk_fp8_f32 v146, v234, v235 op_sel:[0,0,1]
	v_cvt_pk_fp8_f32 v147, v238, v239 op_sel:[0,0,1]
	v_max_f32_e32 v96, v81, v81
	v_max_f32_e32 v97, v80, v80
	v_max_f32_e32 v96, v97, v96
	v_max3_f32 v96, v96, v82, v83
	v_max3_f32 v96, v96, v84, v85
	v_max3_f32 v96, v96, v86, v87
	v_max3_f32 v96, v96, v88, v89
	v_max3_f32 v96, v96, v90, v91
	v_max3_f32 v96, v96, v92, v93
	v_max3_f32 v96, v96, v94, v95
	v_mov_b32_e32 v97, v96
	s_nop 1
	v_permlane32_swap_b32_e32 v96, v97
	v_max_f32_e32 v97, v97, v97
	v_max_f32_e32 v96, v96, v96
	v_max_f32_e32 v96, v96, v97
	v_fma_f32 v97, v96, s38, -v194
	v_cmp_ge_f32_e64 s[4:5], s68, v97
	v_add3_u32 v97, s23, v210, v190
	s_waitcnt vmcnt(1)
	ds_write_b128 v97, v[168:171]
	s_and_saveexec_b64 s[18:19], s[0:1]
	v_add3_u32 v97, s23, v216, v192
	ds_write_b128 v97, v[164:167]
	s_or_b64 exec, exec, s[18:19]
	s_cmpk_gt_u32 s17, 0x83
	s_cselect_b64 s[18:19], -1, 0
	v_lshl_add_u32 v97, s22, 14, v211
	s_and_b64 vcc, exec, s[18:19]
	s_waitcnt vmcnt(0)
	ds_write_b128 v97, v[172:175]
	s_cbranch_vccnz .LBB0_1886
	s_cmpk_lt_u32 s17, 0x7c
	s_cselect_b32 s22, 0, 0xffffffc0
	s_cselect_b32 s23, s74, s75
	s_add_i32 s22, s22, s76
	s_lshl_b32 s26, s22, 6
	s_add_i32 s26, s26, s23
	v_add_u32_e32 v97, s26, v189
	v_mad_i64_i32 v[98:99], s[22:23], v97, s62, v[196:197]
	global_load_dwordx4 v[168:171], v[98:99], off
	s_and_saveexec_b64 s[22:23], s[0:1]
	s_cbranch_execz .LBB0_1885
	v_add_u32_e32 v97, s26, v212
	v_mad_i64_i32 v[98:99], s[28:29], v97, s62, v[198:199]
	global_load_dwordx4 v[164:167], v[98:99], off
